# attention key loop softmax row-sum: 13 SLP-packed v_pk_add_f32 replaced by 19 scalar v_add_f32 (same association; packed fp32 is the slower form beside MFMAs)
# speedup vs baseline: 1.0026x; 1.0026x over previous
.LBB0_277:
	v_exp_f32_e32 v208, v144
	v_exp_f32_e32 v209, v160
	v_exp_f32_e32 v0, v145
	v_exp_f32_e32 v2, v161
	v_exp_f32_e32 v225, v162
	v_add_f32_e32 v3, v209, v208
	v_exp_f32_e32 v8, v163
	v_add_f32_e32 v4, v2, v0
	v_add_f32_e32 v5, v3, v1
	v_exp_f32_e32 v3, v146
	v_add_f32_e32 v5, v4, v5
	v_exp_f32_e32 v4, v147
	v_exp_f32_e32 v160, v165
	v_add_f32_e32 v9, v225, v3
	v_exp_f32_e32 v162, v167
	v_add_f32_e32 v6, v8, v4
	v_add_f32_e32 v7, v9, v5
	v_exp_f32_e32 v5, v148
	v_add_f32_e32 v7, v6, v7
	v_exp_f32_e32 v9, v164
	v_exp_f32_e32 v6, v149
	v_exp_f32_e32 v164, v171
	v_cvt_pk_bf16_f32 v147, v3, v4
	v_add_f32_e32 v161, v9, v5
	v_add_f32_e32 v10, v160, v6
	v_add_f32_e32 v11, v161, v7
	v_exp_f32_e32 v7, v150
	v_add_f32_e32 v11, v10, v11
	v_exp_f32_e32 v161, v166
	v_exp_f32_e32 v10, v151
	v_exp_f32_e32 v150, v169
	v_cvt_pk_bf16_f32 v148, v5, v6
	v_add_f32_e32 v163, v161, v7
	v_add_f32_e32 v12, v162, v10
	v_add_f32_e32 v13, v163, v11
	v_exp_f32_e32 v11, v152
	v_add_f32_e32 v13, v12, v13
	v_exp_f32_e32 v163, v168
	v_exp_f32_e32 v12, v153
	v_cvt_pk_bf16_f32 v149, v7, v10
	v_cvt_pk_bf16_f32 v6, v209, v2
	v_add_f32_e32 v151, v163, v11
	v_add_f32_e32 v144, v150, v12
	v_add_f32_e32 v145, v151, v13
	v_exp_f32_e32 v13, v154
	v_add_f32_e32 v153, v144, v145
	v_exp_f32_e32 v151, v170
	v_exp_f32_e32 v152, v155
	v_cvt_pk_bf16_f32 v10, v11, v12
	v_cvt_pk_bf16_f32 v2, v163, v150
	v_add_f32_e32 v165, v151, v13
	v_add_f32_e32 v144, v164, v152
	v_add_f32_e32 v145, v165, v153
	v_exp_f32_e32 v153, v156
	v_add_f32_e32 v155, v144, v145
	v_exp_f32_e32 v165, v172
	v_exp_f32_e32 v154, v157
	v_cvt_pk_bf16_f32 v11, v13, v152
	v_cvt_pk_bf16_f32 v3, v151, v164
	v_add_f32_e32 v167, v165, v153
	v_cvt_pk_bf16_f32 v12, v153, v154
	ds_read_b64_tr_b16 v[150:151], v228
	ds_read_b64_tr_b16 v[152:153], v230
	v_cvt_pk_bf16_f32 v146, v208, v0
	v_exp_f32_e32 v166, v173
	v_cvt_pk_bf16_f32 v7, v225, v8
	s_waitcnt lgkmcnt(0)
	v_mfma_f32_32x32x16_bf16 v[128:143], v[150:153], v[146:149], v[128:143]
	ds_read_b64_tr_b16 v[150:151], v237
	ds_read_b64_tr_b16 v[152:153], v233
	v_add_f32_e64 v144, v166, v154
	v_add_f32_e64 v145, v167, v155
	v_exp_f32_e32 v155, v158
	v_add_f32_e32 v157, v144, v145
	v_exp_f32_e32 v156, v159
	v_cvt_pk_bf16_f32 v8, v9, v160
	v_cvt_pk_bf16_f32 v9, v161, v162
	s_waitcnt lgkmcnt(0)
	v_mfma_f32_32x32x16_bf16 v[112:127], v[150:153], v[146:149], v[112:127]
	ds_read_b64_tr_b16 v[150:151], v238
	ds_read_b64_tr_b16 v[152:153], v232
	v_cvt_pk_bf16_f32 v13, v155, v156
	v_exp_f32_e32 v158, v174
	v_exp_f32_e32 v168, v175
	v_cvt_pk_bf16_f32 v4, v165, v166
	v_max_f32_e32 v0, v219, v219
	v_add_f32_e32 v169, v158, v155
	s_waitcnt lgkmcnt(0)
	v_mfma_f32_32x32x16_bf16 v[96:111], v[150:153], v[146:149], v[96:111]
	ds_read_b64_tr_b16 v[150:151], v236
	ds_read_b64_tr_b16 v[152:153], v224
	v_cvt_pk_bf16_f32 v5, v158, v168
	v_add_f32_e64 v144, v168, v156
	v_add_f32_e64 v145, v169, v157
	v_add_f32_e32 v144, v144, v145
	v_add_f32_e32 v15, v15, v144
	s_waitcnt lgkmcnt(0)
	v_mfma_f32_32x32x16_bf16 v[80:95], v[150:153], v[146:149], v[80:95]
	ds_read_b64_tr_b16 v[150:151], v228 offset:16384
	ds_read_b64_tr_b16 v[152:153], v230 offset:16384
	s_waitcnt lgkmcnt(0)
	v_mfma_f32_32x32x16_bf16 v[64:79], v[150:153], v[146:149], v[64:79]
	ds_read_b64_tr_b16 v[150:151], v237 offset:16384
	ds_read_b64_tr_b16 v[152:153], v233 offset:16384
	s_waitcnt lgkmcnt(0)
	v_mfma_f32_32x32x16_bf16 v[48:63], v[150:153], v[146:149], v[48:63]
	ds_read_b64_tr_b16 v[150:151], v238 offset:16384
	ds_read_b64_tr_b16 v[152:153], v232 offset:16384
	s_waitcnt lgkmcnt(0)
	v_mfma_f32_32x32x16_bf16 v[32:47], v[150:153], v[146:149], v[32:47]
	ds_read_b64_tr_b16 v[150:151], v236 offset:16384
	ds_read_b64_tr_b16 v[152:153], v224 offset:16384
	s_waitcnt lgkmcnt(0)
	v_mfma_f32_32x32x16_bf16 v[16:31], v[150:153], v[146:149], v[16:31]
	ds_read_b64_tr_b16 v[146:147], v228 offset:4096
	ds_read_b64_tr_b16 v[148:149], v230 offset:4096
	s_waitcnt lgkmcnt(0)
	v_mfma_f32_32x32x16_bf16 v[128:143], v[146:149], v[10:13], v[128:143]
	ds_read_b64_tr_b16 v[146:147], v237 offset:4096
	ds_read_b64_tr_b16 v[148:149], v233 offset:4096
	s_waitcnt lgkmcnt(0)
	v_mfma_f32_32x32x16_bf16 v[112:127], v[146:149], v[10:13], v[112:127]
	ds_read_b64_tr_b16 v[146:147], v238 offset:4096
	ds_read_b64_tr_b16 v[148:149], v232 offset:4096
	s_waitcnt lgkmcnt(0)
	v_mfma_f32_32x32x16_bf16 v[96:111], v[146:149], v[10:13], v[96:111]
	ds_read_b64_tr_b16 v[146:147], v236 offset:4096
	ds_read_b64_tr_b16 v[148:149], v224 offset:4096
	s_waitcnt lgkmcnt(0)
	v_mfma_f32_32x32x16_bf16 v[80:95], v[146:149], v[10:13], v[80:95]
	ds_read_b64_tr_b16 v[146:147], v228 offset:20480
	ds_read_b64_tr_b16 v[148:149], v230 offset:20480
	s_waitcnt lgkmcnt(0)
	v_mfma_f32_32x32x16_bf16 v[64:79], v[146:149], v[10:13], v[64:79]
	ds_read_b64_tr_b16 v[146:147], v237 offset:20480
	ds_read_b64_tr_b16 v[148:149], v233 offset:20480
	s_waitcnt lgkmcnt(0)
	v_mfma_f32_32x32x16_bf16 v[48:63], v[146:149], v[10:13], v[48:63]
	ds_read_b64_tr_b16 v[146:147], v238 offset:20480
	ds_read_b64_tr_b16 v[148:149], v232 offset:20480
	s_waitcnt lgkmcnt(0)
	v_mfma_f32_32x32x16_bf16 v[32:47], v[146:149], v[10:13], v[32:47]
	ds_read_b64_tr_b16 v[146:147], v236 offset:20480
	ds_read_b64_tr_b16 v[148:149], v224 offset:20480
	s_waitcnt lgkmcnt(0)
	v_mfma_f32_32x32x16_bf16 v[16:31], v[146:149], v[10:13], v[16:31]
	ds_read_b64_tr_b16 v[10:11], v228 offset:8192
	ds_read_b64_tr_b16 v[12:13], v230 offset:8192
	s_waitcnt lgkmcnt(0)
	v_mfma_f32_32x32x16_bf16 v[128:143], v[10:13], v[6:9], v[128:143]
	ds_read_b64_tr_b16 v[10:11], v237 offset:8192
	ds_read_b64_tr_b16 v[12:13], v233 offset:8192
	s_waitcnt lgkmcnt(0)
	v_mfma_f32_32x32x16_bf16 v[112:127], v[10:13], v[6:9], v[112:127]
	ds_read_b64_tr_b16 v[10:11], v238 offset:8192
	ds_read_b64_tr_b16 v[12:13], v232 offset:8192
	s_waitcnt lgkmcnt(0)
	v_mfma_f32_32x32x16_bf16 v[96:111], v[10:13], v[6:9], v[96:111]
	ds_read_b64_tr_b16 v[10:11], v236 offset:8192
	ds_read_b64_tr_b16 v[12:13], v224 offset:8192
	s_waitcnt lgkmcnt(0)
	v_mfma_f32_32x32x16_bf16 v[80:95], v[10:13], v[6:9], v[80:95]
	ds_read_b64_tr_b16 v[10:11], v228 offset:24576
	ds_read_b64_tr_b16 v[12:13], v230 offset:24576
	s_waitcnt lgkmcnt(0)
	v_mfma_f32_32x32x16_bf16 v[64:79], v[10:13], v[6:9], v[64:79]
	ds_read_b64_tr_b16 v[10:11], v237 offset:24576
	ds_read_b64_tr_b16 v[12:13], v233 offset:24576
	s_waitcnt lgkmcnt(0)
	v_mfma_f32_32x32x16_bf16 v[48:63], v[10:13], v[6:9], v[48:63]
	ds_read_b64_tr_b16 v[10:11], v238 offset:24576
	ds_read_b64_tr_b16 v[12:13], v232 offset:24576
	s_waitcnt lgkmcnt(0)
	v_mfma_f32_32x32x16_bf16 v[32:47], v[10:13], v[6:9], v[32:47]
	ds_read_b64_tr_b16 v[10:11], v236 offset:24576
	ds_read_b64_tr_b16 v[12:13], v224 offset:24576
	s_waitcnt lgkmcnt(0)
	v_mfma_f32_32x32x16_bf16 v[16:31], v[10:13], v[6:9], v[16:31]
	ds_read_b64_tr_b16 v[6:7], v228 offset:12288
	ds_read_b64_tr_b16 v[8:9], v230 offset:12288
	s_waitcnt lgkmcnt(0)
	v_mfma_f32_32x32x16_bf16 v[128:143], v[6:9], v[2:5], v[128:143]
	ds_read_b64_tr_b16 v[6:7], v237 offset:12288
	ds_read_b64_tr_b16 v[8:9], v233 offset:12288
	s_waitcnt lgkmcnt(0)
	v_mfma_f32_32x32x16_bf16 v[112:127], v[6:9], v[2:5], v[112:127]
	ds_read_b64_tr_b16 v[6:7], v238 offset:12288
	ds_read_b64_tr_b16 v[8:9], v232 offset:12288
	s_waitcnt lgkmcnt(0)
	v_mfma_f32_32x32x16_bf16 v[96:111], v[6:9], v[2:5], v[96:111]
	ds_read_b64_tr_b16 v[6:7], v236 offset:12288
	ds_read_b64_tr_b16 v[8:9], v224 offset:12288
	s_waitcnt lgkmcnt(0)
	v_mfma_f32_32x32x16_bf16 v[80:95], v[6:9], v[2:5], v[80:95]
	ds_read_b64_tr_b16 v[6:7], v228 offset:28672
	ds_read_b64_tr_b16 v[8:9], v230 offset:28672
	s_waitcnt lgkmcnt(0)
	v_mfma_f32_32x32x16_bf16 v[64:79], v[6:9], v[2:5], v[64:79]
	ds_read_b64_tr_b16 v[6:7], v237 offset:28672
	ds_read_b64_tr_b16 v[8:9], v233 offset:28672
	s_waitcnt lgkmcnt(0)
	v_mfma_f32_32x32x16_bf16 v[48:63], v[6:9], v[2:5], v[48:63]
	ds_read_b64_tr_b16 v[6:7], v238 offset:28672
	ds_read_b64_tr_b16 v[8:9], v232 offset:28672
	s_waitcnt lgkmcnt(0)
	v_mfma_f32_32x32x16_bf16 v[32:47], v[6:9], v[2:5], v[32:47]
	ds_read_b64_tr_b16 v[6:7], v236 offset:28672
	ds_read_b64_tr_b16 v[8:9], v224 offset:28672
	s_waitcnt lgkmcnt(0)
	v_mfma_f32_32x32x16_bf16 v[16:31], v[6:9], v[2:5], v[16:31]
	v_max_f32_e32 v2, 0, v0
	v_cmp_lt_f32_e32 vcc, 0, v2
	s_cbranch_vccz .LBB0_268
	v_exp_f32_e64 v0, -v2
	v_add_f32_e32 v208, v14, v2
	v_pk_mul_f32 v[142:143], v[0:1], v[142:143] op_sel_hi:[0,1]
	v_pk_mul_f32 v[140:141], v[0:1], v[140:141] op_sel_hi:[0,1]
	v_pk_mul_f32 v[138:139], v[0:1], v[138:139] op_sel_hi:[0,1]
	v_pk_mul_f32 v[136:137], v[0:1], v[136:137] op_sel_hi:[0,1]
	v_pk_mul_f32 v[134:135], v[0:1], v[134:135] op_sel_hi:[0,1]
	v_pk_mul_f32 v[132:133], v[0:1], v[132:133] op_sel_hi:[0,1]
	v_pk_mul_f32 v[130:131], v[0:1], v[130:131] op_sel_hi:[0,1]
	v_pk_mul_f32 v[128:129], v[0:1], v[128:129] op_sel_hi:[0,1]
	v_pk_mul_f32 v[126:127], v[0:1], v[126:127] op_sel_hi:[0,1]
	v_pk_mul_f32 v[124:125], v[0:1], v[124:125] op_sel_hi:[0,1]
	v_pk_mul_f32 v[122:123], v[0:1], v[122:123] op_sel_hi:[0,1]
	v_pk_mul_f32 v[120:121], v[0:1], v[120:121] op_sel_hi:[0,1]
	v_pk_mul_f32 v[118:119], v[0:1], v[118:119] op_sel_hi:[0,1]
	v_pk_mul_f32 v[116:117], v[0:1], v[116:117] op_sel_hi:[0,1]
	v_pk_mul_f32 v[114:115], v[0:1], v[114:115] op_sel_hi:[0,1]
	v_pk_mul_f32 v[112:113], v[0:1], v[112:113] op_sel_hi:[0,1]
	v_pk_mul_f32 v[110:111], v[0:1], v[110:111] op_sel_hi:[0,1]
	v_pk_mul_f32 v[108:109], v[0:1], v[108:109] op_sel_hi:[0,1]
	v_pk_mul_f32 v[106:107], v[0:1], v[106:107] op_sel_hi:[0,1]
	v_pk_mul_f32 v[104:105], v[0:1], v[104:105] op_sel_hi:[0,1]
	v_pk_mul_f32 v[102:103], v[0:1], v[102:103] op_sel_hi:[0,1]
	v_pk_mul_f32 v[100:101], v[0:1], v[100:101] op_sel_hi:[0,1]
	v_pk_mul_f32 v[98:99], v[0:1], v[98:99] op_sel_hi:[0,1]
	v_pk_mul_f32 v[96:97], v[0:1], v[96:97] op_sel_hi:[0,1]
	v_pk_mul_f32 v[94:95], v[0:1], v[94:95] op_sel_hi:[0,1]
	v_pk_mul_f32 v[92:93], v[0:1], v[92:93] op_sel_hi:[0,1]
	v_pk_mul_f32 v[90:91], v[0:1], v[90:91] op_sel_hi:[0,1]
	v_pk_mul_f32 v[88:89], v[0:1], v[88:89] op_sel_hi:[0,1]
	v_pk_mul_f32 v[86:87], v[0:1], v[86:87] op_sel_hi:[0,1]
	v_pk_mul_f32 v[84:85], v[0:1], v[84:85] op_sel_hi:[0,1]
	v_pk_mul_f32 v[82:83], v[0:1], v[82:83] op_sel_hi:[0,1]
	v_pk_mul_f32 v[80:81], v[0:1], v[80:81] op_sel_hi:[0,1]
	v_pk_mul_f32 v[78:79], v[0:1], v[78:79] op_sel_hi:[0,1]
	v_pk_mul_f32 v[76:77], v[0:1], v[76:77] op_sel_hi:[0,1]
	v_pk_mul_f32 v[74:75], v[0:1], v[74:75] op_sel_hi:[0,1]
	v_pk_mul_f32 v[72:73], v[0:1], v[72:73] op_sel_hi:[0,1]
	v_pk_mul_f32 v[70:71], v[0:1], v[70:71] op_sel_hi:[0,1]
	v_pk_mul_f32 v[68:69], v[0:1], v[68:69] op_sel_hi:[0,1]
	v_pk_mul_f32 v[66:67], v[0:1], v[66:67] op_sel_hi:[0,1]
	v_pk_mul_f32 v[64:65], v[0:1], v[64:65] op_sel_hi:[0,1]
	v_pk_mul_f32 v[62:63], v[0:1], v[62:63] op_sel_hi:[0,1]
	v_pk_mul_f32 v[60:61], v[0:1], v[60:61] op_sel_hi:[0,1]
	v_pk_mul_f32 v[58:59], v[0:1], v[58:59] op_sel_hi:[0,1]
	v_pk_mul_f32 v[56:57], v[0:1], v[56:57] op_sel_hi:[0,1]
	v_pk_mul_f32 v[54:55], v[0:1], v[54:55] op_sel_hi:[0,1]
	v_pk_mul_f32 v[52:53], v[0:1], v[52:53] op_sel_hi:[0,1]
	v_pk_mul_f32 v[50:51], v[0:1], v[50:51] op_sel_hi:[0,1]
	v_pk_mul_f32 v[48:49], v[0:1], v[48:49] op_sel_hi:[0,1]
	v_pk_mul_f32 v[46:47], v[0:1], v[46:47] op_sel_hi:[0,1]
	v_pk_mul_f32 v[44:45], v[0:1], v[44:45] op_sel_hi:[0,1]
	v_pk_mul_f32 v[42:43], v[0:1], v[42:43] op_sel_hi:[0,1]
	v_pk_mul_f32 v[40:41], v[0:1], v[40:41] op_sel_hi:[0,1]
	v_pk_mul_f32 v[38:39], v[0:1], v[38:39] op_sel_hi:[0,1]
	v_pk_mul_f32 v[36:37], v[0:1], v[36:37] op_sel_hi:[0,1]
	v_pk_mul_f32 v[34:35], v[0:1], v[34:35] op_sel_hi:[0,1]
	v_pk_mul_f32 v[32:33], v[0:1], v[32:33] op_sel_hi:[0,1]
	v_pk_mul_f32 v[30:31], v[0:1], v[30:31] op_sel_hi:[0,1]
	v_pk_mul_f32 v[28:29], v[0:1], v[28:29] op_sel_hi:[0,1]
	v_pk_mul_f32 v[26:27], v[0:1], v[26:27] op_sel_hi:[0,1]
	v_pk_mul_f32 v[24:25], v[0:1], v[24:25] op_sel_hi:[0,1]
	v_pk_mul_f32 v[22:23], v[0:1], v[22:23] op_sel_hi:[0,1]
	v_pk_mul_f32 v[20:21], v[0:1], v[20:21] op_sel_hi:[0,1]
	v_pk_mul_f32 v[18:19], v[0:1], v[18:19] op_sel_hi:[0,1]
	v_pk_mul_f32 v[16:17], v[0:1], v[16:17] op_sel_hi:[0,1]
	v_mul_f32_e32 v15, v0, v15
	s_add_i32 s18, s18, 64
	s_cmp_eq_u32 s21, s12
	v_add_u32_e32 v249, 64, v249
	s_cbranch_scc0 .LBB0_269
